# ssd_out+attention phase (layers 0-2): odd workgroups run attention first and ssd_out second so the two halves of the grid stream ssd_out data at different times
# baseline (speedup 1.0000x reference)
.LBB0_1231:
	s_andn2_b64 vcc, exec, s[0:1]
	s_cbranch_vccnz .LBB0_1347
	s_mov_b32 s16, 0
	s_nop 0
	v_writelane_b32 v255, s16, 51
.Lk3_again:
	v_readlane_b32 s0, v251, 10
	v_readlane_b32 s1, v251, 11
	v_readlane_b32 s2, v251, 12
	v_readlane_b32 s3, v251, 13
	s_waitcnt vmcnt(15)
	v_mbcnt_lo_u32_b32 v0, -1, 0
	v_mbcnt_hi_u32_b32 v0, -1, v0
	s_mov_b64 s[0:1], s[2:3]
	v_add_u32_e32 v219, s95, v0
	s_add_u32 s2, s0, 0x28600000
	s_addc_u32 s3, s1, 0
	s_add_u32 s6, s0, 0x3a600000
	s_addc_u32 s7, s1, 0
	s_add_u32 s8, s0, 0x3ae00000
	s_addc_u32 s9, s1, 0
	s_add_u32 s12, s0, 0x41200000
	s_addc_u32 s13, s1, 0
	s_add_u32 s10, s0, 0x51200000
	s_addc_u32 s11, s1, 0
	s_add_u32 s24, s0, 0x5d200000
	s_addc_u32 s25, s1, 0
	s_add_u32 s4, s0, 0x5db00000
	s_addc_u32 s5, s1, 0
	v_readlane_b32 s14, v254, 8
	s_mov_b64 s[0:1], -1
	s_cmp_eq_u32 s14, 3
	v_and_b32_e32 v166, 15, v219
	v_lshlrev_b32_e32 v220, 3, v219
	v_readlane_b32 s15, v254, 9
	s_cbranch_scc1 .LBB0_1264
	v_readlane_b32 s0, v253, 4
	v_readlane_b32 s1, v253, 5
	v_readfirstlane_b32 s14, v219
	v_readlane_b32 s16, v255, 51
	s_cmp_lg_u32 s16, 0
	s_cbranch_scc1 .Lk3_normal
	s_bitcmp1_b32 s83, 0
	s_cbranch_scc0 .Lk3_normal
	s_mov_b32 s16, 1
	s_nop 0
	v_writelane_b32 v255, s16, 51
	s_branch .Lk3_attnfirst
.Lk3_normal:
	s_andn2_b64 vcc, exec, s[0:1]
	s_mov_b64 s[0:1], -1
	s_cbranch_vccnz .LBB0_1235
.Lk3_attnfirst:
	v_lshlrev_b32_e32 v168, 4, v219
	v_lshrrev_b32_e32 v163, 2, v166
	s_mov_b64 s[0:1], 0

.LBB0_1247:
	v_readlane_b32 s0, v255, 51
	s_cmp_eq_u32 s0, 2
	s_cbranch_scc1 .LBB0_1263
	v_readlane_b32 s0, v251, 54
	v_readlane_b32 s1, v251, 55
	s_andn2_b64 vcc, exec, s[0:1]
	v_readfirstlane_b32 s0, v219
	s_waitcnt lgkmcnt(0)
	s_barrier
	s_cbranch_vccnz .LBB0_1263
	v_bfe_u32 v3, v219, 4, 2
	v_lshrrev_b32_e32 v2, 4, v219
	v_lshlrev_b32_e32 v0, 3, v3
	v_mov_b32_e32 v1, v33
	v_lshlrev_b32_e32 v170, 2, v3
	v_lshl_add_u64 v[172:173], s[4:5], 0, v[0:1]
	v_bitop3_b32 v1, v2, v166, 3 bitop3:0x6c
	s_waitcnt vmcnt(14)
	v_lshrrev_b32_e32 v4, 2, v219
	v_or_b32_e32 v5, v170, v163
	v_lshlrev_b32_e32 v222, 4, v1
	v_bitop3_b32 v1, v3, v166, 4 bitop3:0x36
	v_and_or_b32 v4, v4, 4, v163
	v_lshlrev_b32_e32 v5, 8, v5
	v_and_b32_e32 v6, 8, v220
	v_lshlrev_b32_e32 v223, 4, v1
	v_bitop3_b32 v1, v3, v166, 8 bitop3:0x36
	v_lshlrev_b32_e32 v4, 1, v4
	v_add3_u32 v221, 0, v5, v6
	v_bfe_u32 v5, v219, 1, 1
	v_lshlrev_b32_e32 v224, 4, v1
	v_bitop3_b32 v1, v3, v166, 12 bitop3:0x36
	v_lshlrev_b32_e32 v225, 4, v1
	v_or_b32_e32 v1, v4, v5
	v_lshlrev_b32_e32 v237, 4, v1
	v_bitop3_b32 v1, v4, v5, 2 bitop3:0x1e
	v_lshlrev_b32_e32 v238, 4, v1
	v_bitop3_b32 v1, v4, v5, 4 bitop3:0x1e
	v_lshlrev_b32_e32 v239, 4, v1
	v_bitop3_b32 v1, v4, v5, 6 bitop3:0x1e
	v_lshlrev_b32_e32 v240, 4, v1
	v_bitop3_b32 v1, v4, v5, 8 bitop3:0x1e
	v_lshlrev_b32_e32 v241, 4, v1
	v_bitop3_b32 v1, v4, v5, 10 bitop3:0x1e
	v_lshlrev_b32_e32 v242, 4, v1
	v_bitop3_b32 v1, v4, v5, 12 bitop3:0x1e
	s_ashr_i32 s14, s0, 6
	v_lshlrev_b32_e32 v243, 4, v1
	v_bitop3_b32 v1, v4, v5, 14 bitop3:0x1e
	s_lshl_b32 s15, s14, 3
	v_lshlrev_b32_e32 v244, 4, v1
	v_or_b32_e32 v1, s15, v3
	v_lshlrev_b32_e32 v4, 3, v166
	v_lshlrev_b32_e32 v5, 4, v3
	s_and_b32 s20, s0, 0xffffff80
	s_lshl_b32 s0, s14, 5
	v_xor_b32_e32 v4, v5, v4
	v_or_b32_e32 v5, 4, v1
	v_and_or_b32 v245, s0, 32, v166
	v_mad_i64_i32 v[180:181], s[0:1], v1, s96, 0
	v_mad_i64_i32 v[182:183], s[0:1], v5, s96, 0
	v_bitop3_b32 v1, v1, v219, 4 bitop3:0x36
	v_lshlrev_b32_e32 v1, 3, v1
	s_lshl_b32 s0, s14, 14
	v_bitop3_b32 v2, s15, v219, v3 bitop3:0x36
	v_and_b32_e32 v6, 0x78, v1
	v_lshlrev_b32_e32 v1, 1, v5
	s_and_b32 s0, s0, 0x4000
	s_lshl_b32 s16, s14, 11
	v_lshlrev_b32_e32 v2, 3, v2
	v_bitop3_b32 v1, v1, v166, 14 bitop3:0x6c
	s_add_i32 s0, s0, 0
	v_add_u32_e32 v174, 0x2000, v168
	v_add_u32_e32 v176, 0x4000, v168
	v_add_u32_e32 v178, 0x6000, v168
	v_and_b32_e32 v2, 0x78, v2
	s_add_i32 s21, s16, 0
	s_waitcnt vmcnt(13)
	v_lshlrev_b32_e32 v8, 3, v1
	s_add_i32 s0, s0, 0x10000
	s_addk_i32 s15, 0x44
	v_lshl_add_u32 v171, v166, 8, 0
	v_ashrrev_i32_e32 v169, 31, v168
	v_ashrrev_i32_e32 v175, 31, v174
	v_ashrrev_i32_e32 v177, 31, v176
	v_ashrrev_i32_e32 v179, 31, v178
	v_lshl_add_u32 v246, v166, 9, s0
	v_or_b32_e32 v247, s15, v3
	v_lshlrev_b32_e32 v32, 1, v2
	v_lshlrev_b32_e32 v184, 1, v4
	v_lshlrev_b32_e32 v186, 1, v6
	v_lshlrev_b32_e32 v188, 1, v8
	v_add3_u32 v32, v180, v32, s84
	v_add3_u32 v184, v180, v184, s90
	v_add3_u32 v186, v182, v186, s84
	v_add3_u32 v188, v182, v188, s90
	v_lshlrev_b32_e32 v190, 1, v0
	s_add_i32 s22, s21, 0x8400
	s_mov_b32 s23, s83
	s_branch .LBB0_1250

.LBB0_1263:
	s_mov_b64 s[0:1], 0
	s_barrier
	v_readlane_b32 s2, v255, 51
	s_cmp_eq_u32 s2, 1
	s_cbranch_scc0 .Lk3_done
	s_mov_b32 s2, 2
	s_nop 0
	v_writelane_b32 v255, s2, 51
	s_branch .Lk3_again
.Lk3_done:
.LBB0_1264:
	s_and_b64 vcc, exec, s[0:1]
	s_cbranch_vccz .LBB0_1293
	v_readlane_b32 s14, v254, 13
	v_readlane_b32 s15, v254, 14
	v_bfe_u32 v159, v219, 4, 2
	v_readfirstlane_b32 s0, v219
	s_and_b64 vcc, exec, s[14:15]
	v_lshlrev_b32_e32 v168, 4, v219
	v_lshrrev_b32_e32 v167, 2, v166
	v_lshlrev_b32_e32 v158, 3, v159
	v_lshlrev_b32_e32 v170, 2, v159
	s_cbranch_vccnz .LBB0_1276
	v_and_b32_e32 v169, 63, v219
	v_lshlrev_b32_e32 v1, 2, v169
	v_add_u32_e32 v2, 0xfc, v1
	s_ashr_i32 s22, s0, 6
	s_andn2_b32 s0, s0, 63
	v_and_b32_e32 v175, 0xfc, v2
	v_add_u32_e32 v2, 0xf8, v1
	s_lshl_b32 s23, s0, 2
	s_mul_i32 s14, s22, 0x2800
	v_and_b32_e32 v177, 0xfc, v2
	v_add_u32_e32 v2, 0xf0, v1
	s_add_i32 s0, s23, 0
	s_add_i32 s14, s14, 0
	v_and_b32_e32 v32, 0x70, v168
	v_and_b32_e32 v179, 0xfc, v2
	v_add_u32_e32 v2, 0xe0, v1
	s_add_i32 s1, s0, 0x14800
	s_add_i32 s0, s0, 0x14000
	v_lshl_add_u64 v[160:161], s[8:9], 0, v[32:33]
	v_add_u32_e32 v0, s14, v32
	v_and_b32_e32 v180, 0xfc, v2
	v_add_u32_e32 v2, 0xc0, v1
	v_and_b32_e32 v32, 48, v219
	s_waitcnt vmcnt(14)
	v_or_b32_e32 v6, 2, v170
	v_bfe_u32 v171, v219, 3, 3
	v_and_b32_e32 v181, 0xfc, v2
	v_xor_b32_e32 v182, 0x80, v1
	v_add_u32_e32 v183, s0, v1
	v_add_u32_e32 v184, s1, v1
	v_lshl_add_u64 v[162:163], s[12:13], 0, v[32:33]
	v_or_b32_e32 v1, v170, v167
	v_mov_b32_e32 v2, s14
	s_movk_i32 s14, 0xa0
	v_readlane_b32 s12, v253, 11
	s_waitcnt lgkmcnt(0)
	v_or_b32_e32 v5, 3, v170
	v_lshlrev_b32_e32 v7, 2, v6
	v_mad_u32_u24 v1, v1, s14, v2
	v_and_b32_e32 v3, 24, v220
	v_readlane_b32 s13, v253, 12
	v_mul_u32_u24_e32 v4, 0xa0, v171
	v_add_u32_e32 v188, s1, v7
	v_add_u32_e32 v189, s0, v7
	v_lshlrev_b32_e32 v7, 2, v5
	v_mad_u32_u24 v192, v166, s14, v2
	s_mov_b32 s26, 0
	v_cmp_eq_u32_e32 vcc, 0, v169
	v_cmp_gt_u32_e64 s[36:37], 2, v169
	v_cmp_gt_u32_e64 s[38:39], 4, v169
	v_cmp_gt_u32_e64 s[40:41], 8, v169
	v_cmp_gt_u32_e64 s[42:43], 16, v169
	v_cmp_gt_u32_e64 s[44:45], 32, v169
	v_lshl_add_u32 v185, v166, 2, s1
	v_lshl_add_u64 v[164:165], s[12:13], 0, v[32:33]
	v_add_u32_e32 v186, s1, v32
	v_add_u32_e32 v187, s0, v32
	v_add_u32_e32 v190, s1, v7
	v_add_u32_e32 v191, s0, v7
	v_cmp_gt_u32_e64 s[46:47], v170, v166
	v_cmp_lt_u32_e64 s[48:49], v170, v166
	v_cmp_gt_u32_e64 s[50:51], v5, v166
	v_cmp_gt_u32_e64 s[52:53], v6, v166
	v_or_b32_e32 v193, 32, v158
	v_or_b32_e32 v194, 64, v158
	v_or_b32_e32 v195, 0x60, v158
	v_or_b32_e32 v196, 16, v166
	v_add_u32_e32 v197, 0xa00, v192
	v_or_b32_e32 v208, 32, v166
	v_add_u32_e32 v209, 0x1400, v192
	v_or_b32_e32 v210, 48, v166
	v_add_u32_e32 v211, 0x1e00, v192
	v_add_u32_e32 v212, v0, v4
	v_add_u32_e32 v213, v1, v3
	s_mov_b32 s27, s83
	s_branch .LBB0_1268
